# baseline (speedup 1.0000x reference)
_Z16sum_layer_kernelPKfS0_Pf:
	s_load_dwordx4 s[4:7], s[0:1], 0x0
	s_load_dwordx2 s[8:9], s[0:1], 0x10
	v_bfe_u32 v41, v0, 5, 1
	v_and_b32_e32 v40, 31, v0
	s_lshl_b32 s0, s2, 10
	v_lshlrev_b32_e32 v1, 9, v41
	v_or3_b32 v1, v1, s0, v40
	s_waitcnt lgkmcnt(0)
	s_and_b32 s13, s7, 0xffff
	s_mov_b32 s15, 0x20000
	s_mov_b32 s14, 0x200000
	s_mov_b32 s12, s6
	v_lshlrev_b32_e32 v1, 2, v1
	buffer_load_dword v18, v1, s[12:15], 0 offen nt
	buffer_load_dword v19, v1, s[12:15], 0 offen offset:128 nt
	buffer_load_dword v20, v1, s[12:15], 0 offen offset:256 nt
	buffer_load_dword v21, v1, s[12:15], 0 offen offset:384 nt
	buffer_load_dword v22, v1, s[12:15], 0 offen offset:512 nt
	buffer_load_dword v23, v1, s[12:15], 0 offen offset:640 nt
	buffer_load_dword v24, v1, s[12:15], 0 offen offset:768 nt
	buffer_load_dword v25, v1, s[12:15], 0 offen offset:896 nt
	buffer_load_dword v26, v1, s[12:15], 0 offen offset:1024 nt
	buffer_load_dword v27, v1, s[12:15], 0 offen offset:1152 nt
	buffer_load_dword v28, v1, s[12:15], 0 offen offset:1280 nt
	buffer_load_dword v29, v1, s[12:15], 0 offen offset:1408 nt
	buffer_load_dword v30, v1, s[12:15], 0 offen offset:1536 nt
	buffer_load_dword v31, v1, s[12:15], 0 offen offset:1664 nt
	buffer_load_dword v32, v1, s[12:15], 0 offen offset:1792 nt
	s_nop 0
	buffer_load_dword v1, v1, s[12:15], 0 offen offset:1920 nt
	v_lshrrev_b32_e32 v42, 6, v0
	s_lshl_b32 s0, s2, 5
	v_lshlrev_b32_e32 v3, 2, v0
	v_lshl_add_u32 v2, v42, 19, s0
	v_and_b32_e32 v34, 28, v3
	v_or_b32_e32 v2, v2, v34
	v_bfe_u32 v33, v0, 3, 3
	v_lshlrev_b32_e32 v2, 2, v2
	s_and_b32 s5, s5, 0xffff
	s_mov_b32 s6, 0x800000
	s_mov_b32 s7, s15
	s_and_b32 s9, s9, 0xffff
	s_mov_b32 s10, s6
	s_mov_b32 s11, s15
	s_mov_b32 s16, 0x80000
	s_mov_b32 s17, 0x100000
	s_mov_b32 s18, 0x180000
	v_lshl_add_u32 v35, v33, 16, v2
	v_mov_b32_e32 v60, v35
	s_mov_b32 s0, 0x80000
	buffer_load_dwordx4 v[2:5], v35, s[4:7], 0 offen nt
	buffer_load_dwordx4 v[6:9], v35, s[4:7], s0 offen nt
	s_mov_b32 s0, 0x100000
	s_mov_b32 s1, 0x180000
	buffer_load_dwordx4 v[10:13], v35, s[4:7], s0 offen nt
	buffer_load_dwordx4 v[14:17], v35, s[4:7], s1 offen nt
	v_and_b32_e32 v35, 63, v0
	s_waitcnt vmcnt(18)
	v_max_f32_e32 v0, v19, v19
	v_max_f32_e32 v36, v18, v18
	v_max_f32_e32 v0, v36, v0
	s_waitcnt vmcnt(16)
	v_max3_f32 v0, v0, v20, v21
	s_waitcnt vmcnt(14)
	v_max3_f32 v0, v0, v22, v23
	s_waitcnt vmcnt(12)
	v_max3_f32 v0, v0, v24, v25
	s_waitcnt vmcnt(10)
	v_max3_f32 v0, v0, v26, v27
	s_waitcnt vmcnt(8)
	v_max3_f32 v0, v0, v28, v29
	s_waitcnt vmcnt(6)
	v_max3_f32 v0, v0, v30, v31
	s_waitcnt vmcnt(4)
	v_max3_f32 v0, v0, v32, v1
	v_mov_b32_e32 v36, v0
	s_nop 1
	v_permlane32_swap_b32_e32 v0, v36
	v_max_f32_e32 v36, v36, v36
	v_max_f32_e32 v0, v0, v0
	v_max_f32_e32 v0, v0, v36
	v_mov_b32_e32 v36, 0xc1600000
	s_mov_b32 s0, 0x3fb8aa3b
	v_fmamk_f32 v0, v0, 0x3fb8aa3b, v36
	v_fma_f32 v18, v18, s0, -v0
	v_exp_f32_e32 v37, v18
	v_fma_f32 v18, v19, s0, -v0
	v_exp_f32_e32 v38, v18
	v_fma_f32 v18, v20, s0, -v0
	v_exp_f32_e32 v20, v18
	v_fma_f32 v18, v21, s0, -v0
	v_exp_f32_e32 v21, v18
	v_fma_f32 v19, v22, s0, -v0
	v_add_f32_e32 v18, 0, v37
	v_exp_f32_e32 v22, v19
	v_fma_f32 v19, v23, s0, -v0
	v_add_f32_e32 v18, v18, v38
	v_exp_f32_e32 v39, v19
	v_fma_f32 v19, v24, s0, -v0
	v_add_f32_e32 v18, v18, v20
	v_exp_f32_e32 v23, v19
	v_fma_f32 v19, v25, s0, -v0
	v_add_f32_e32 v18, v18, v21
	v_exp_f32_e32 v24, v19
	v_fma_f32 v19, v26, s0, -v0
	v_add_f32_e32 v18, v18, v22
	v_exp_f32_e32 v43, v19
	v_fma_f32 v19, v27, s0, -v0
	v_add_f32_e32 v18, v18, v39
	v_exp_f32_e32 v44, v19
	v_fma_f32 v19, v28, s0, -v0
	v_add_f32_e32 v18, v18, v23
	v_exp_f32_e32 v45, v19
	v_fma_f32 v19, v29, s0, -v0
	v_add_f32_e32 v18, v18, v24
	v_exp_f32_e32 v46, v19
	v_fma_f32 v19, v30, s0, -v0
	v_add_f32_e32 v18, v18, v43
	v_exp_f32_e32 v47, v19
	v_fma_f32 v19, v31, s0, -v0
	v_add_f32_e32 v18, v18, v44
	v_exp_f32_e32 v48, v19
	v_fma_f32 v19, v32, s0, -v0
	v_add_f32_e32 v18, v18, v45
	v_exp_f32_e32 v49, v19
	v_fma_f32 v0, v1, s0, -v0
	v_add_f32_e32 v18, v18, v46
	v_exp_f32_e32 v50, v0
	v_add_f32_e32 v0, v18, v47
	v_add_f32_e32 v0, v0, v48
	v_add_f32_e32 v0, v0, v49
	v_add_f32_e32 v0, v0, v50
	v_mov_b32_e32 v1, v0
	s_nop 1
	v_permlane32_swap_b32_e32 v0, v1
	v_add_f32_e32 v0, v0, v1
	v_log_f32_e32 v0, v0
	s_nop 0
	v_add_f32_e32 v0, 0x41600000, v0
	v_mul_f32_e32 v25, 0xbf317218, v0
	v_mul_u32_u24_e32 v0, 0x1200, v42
	v_mul_u32_u24_e32 v1, 0x90, v33
	v_lshlrev_b32_e32 v18, 2, v34
	v_add3_u32 v1, v0, v1, v18
	v_mov_b32_e32 v59, v1
	s_waitcnt vmcnt(3)
	ds_write_b128 v1, v[2:5]
	s_waitcnt vmcnt(2)
	ds_write_b128 v1, v[6:9] offset:1152
	s_waitcnt vmcnt(1)
	ds_write_b128 v1, v[10:13] offset:2304
	s_waitcnt vmcnt(0)
	ds_write_b128 v1, v[14:17] offset:3456
	v_mul_u32_u24_e32 v1, 0x90, v40
	v_lshlrev_b32_e32 v2, 6, v41
	v_add3_u32 v12, v0, v1, v2
	v_lshlrev_b32_e32 v58, 4, v41
	v_add3_u32 v57, v0, v1, v58
	ds_read_b128 v[0:3], v12
	ds_read_b128 v[4:7], v12 offset:16
	ds_read_b128 v[8:11], v12 offset:32
	ds_read_b128 v[16:19], v12 offset:48
	v_cmp_gt_u32_e32 vcc, 32, v35
	s_waitcnt lgkmcnt(3)
	v_max_f32_e32 v12, v1, v1
	v_max_f32_e32 v13, v0, v0
	v_max_f32_e32 v12, v13, v12
	v_max3_f32 v12, v12, v2, v3
	s_waitcnt lgkmcnt(2)
	v_max3_f32 v12, v12, v4, v5
	v_max3_f32 v12, v12, v6, v7
	s_waitcnt lgkmcnt(1)
	v_max3_f32 v12, v12, v8, v9
	v_max3_f32 v12, v12, v10, v11
	s_waitcnt lgkmcnt(0)
	v_max3_f32 v12, v12, v16, v17
	v_max3_f32 v12, v12, v18, v19
	v_mov_b32_e32 v13, v12
	s_nop 1
	v_permlane32_swap_b32_e32 v12, v13
	v_max_f32_e32 v13, v13, v13
	v_max_f32_e32 v12, v12, v12
	v_max_f32_e32 v12, v12, v13
	v_fmac_f32_e32 v36, 0x3fb8aa3b, v12
	v_fma_f32 v0, v0, s0, -v36
	v_cndmask_b32_e64 v13, v25, 1.0, vcc
	v_exp_f32_e32 v25, v0
	v_fma_f32 v0, v1, s0, -v36
	v_exp_f32_e32 v26, v0
	v_fma_f32 v0, v2, s0, -v36
	v_exp_f32_e32 v27, v0
	v_fma_f32 v0, v3, s0, -v36
	v_exp_f32_e32 v28, v0
	v_fma_f32 v0, v4, s0, -v36
	v_exp_f32_e32 v29, v0
	v_fma_f32 v0, v5, s0, -v36
	v_exp_f32_e32 v30, v0
	v_fma_f32 v0, v6, s0, -v36
	v_exp_f32_e32 v31, v0
	v_fma_f32 v0, v7, s0, -v36
	v_exp_f32_e32 v32, v0
	v_fma_f32 v16, v16, s0, -v36
	v_fma_f32 v0, v8, s0, -v36
	v_exp_f32_e32 v34, v16
	v_fma_f32 v16, v17, s0, -v36
	v_exp_f32_e32 v51, v0
	v_fma_f32 v0, v9, s0, -v36
	v_exp_f32_e32 v54, v16
	v_fma_f32 v16, v18, s0, -v36
	v_exp_f32_e32 v52, v0
	v_fma_f32 v0, v10, s0, -v36
	v_exp_f32_e32 v35, v16
	v_fma_f32 v16, v19, s0, -v36
	v_exp_f32_e32 v33, v0
	v_fma_f32 v0, v11, s0, -v36
	v_exp_f32_e32 v36, v16
	v_cvt_pk_f16_f32 v19, v31, v32
	v_cvt_pk_f16_f32 v18, v29, v30
	v_cvt_pk_f16_f32 v17, v27, v28
	v_cvt_pk_f16_f32 v16, v25, v26
	v_cndmask_b32_e32 v1, 1.0, v12, vcc
	v_exp_f32_e32 v53, v0
	v_cvt_pk_f16_f32 v23, v23, v24
	v_cvt_pk_f16_f32 v22, v22, v39
	v_cvt_pk_f16_f32 v21, v20, v21
	v_cvt_pk_f16_f32 v20, v37, v38
	v_cvt_pk_f16_f32 v35, v35, v36
	v_cvt_pk_f16_f32 v34, v34, v54
	v_mfma_f32_32x32x16_f16 v[16:31], v[20:23], v[16:19], 0
	v_cvt_pk_f16_f32 v33, v33, v53
	v_cvt_pk_f16_f32 v32, v51, v52
	v_cvt_pk_f16_f32 v39, v49, v50
	v_cvt_pk_f16_f32 v38, v47, v48
	v_cvt_pk_f16_f32 v37, v45, v46
	v_cvt_pk_f16_f32 v36, v43, v44
	v_mfma_f32_32x32x2_f32 v[0:15], v13, v1, 0
	v_mfma_f32_32x32x16_f16 v[16:31], v[36:39], v[32:35], v[16:31]
	s_mov_b32 s1, 0x3f317218
	s_nop 10
	v_log_f32_e32 v16, v16
	v_log_f32_e32 v17, v17
	v_log_f32_e32 v18, v18
	v_log_f32_e32 v19, v19
	v_log_f32_e32 v20, v20
	v_log_f32_e32 v21, v21
	v_log_f32_e32 v22, v22
	v_log_f32_e32 v23, v23
	v_fmac_f32_e32 v0, s1, v16
	v_fmac_f32_e32 v1, s1, v17
	v_fmac_f32_e32 v2, s1, v18
	v_fmac_f32_e32 v3, s1, v19
	ds_write_b128 v57, v[0:3]
	v_log_f32_e32 v24, v24
	v_log_f32_e32 v25, v25
	v_log_f32_e32 v26, v26
	v_log_f32_e32 v27, v27
	v_fmac_f32_e32 v4, s1, v20
	v_fmac_f32_e32 v5, s1, v21
	v_fmac_f32_e32 v6, s1, v22
	v_fmac_f32_e32 v7, s1, v23
	ds_write_b128 v57, v[4:7] offset:32
	v_log_f32_e32 v28, v28
	v_log_f32_e32 v29, v29
	v_log_f32_e32 v30, v30
	v_log_f32_e32 v31, v31
	v_fmac_f32_e32 v8, s1, v24
	v_fmac_f32_e32 v9, s1, v25
	v_fmac_f32_e32 v10, s1, v26
	v_fmac_f32_e32 v11, s1, v27
	ds_write_b128 v57, v[8:11] offset:64
	v_fmac_f32_e32 v12, s1, v28
	v_fmac_f32_e32 v13, s1, v29
	v_fmac_f32_e32 v14, s1, v30
	v_fmac_f32_e32 v15, s1, v31
	ds_write_b128 v57, v[12:15] offset:96
	ds_read_b128 v[16:19], v59
	ds_read_b128 v[20:23], v59 offset:1152
	ds_read_b128 v[24:27], v59 offset:2304
	ds_read_b128 v[28:31], v59 offset:3456
	s_waitcnt lgkmcnt(3)
	buffer_store_dwordx4 v[16:19], v60, s[8:11], 0 offen sc1
	s_waitcnt lgkmcnt(2)
	buffer_store_dwordx4 v[20:23], v60, s[8:11], s16 offen sc1
	s_waitcnt lgkmcnt(1)
	buffer_store_dwordx4 v[24:27], v60, s[8:11], s17 offen sc1
	s_waitcnt lgkmcnt(0)
	buffer_store_dwordx4 v[28:31], v60, s[8:11], s18 offen sc1
	s_endpgm

	.amdhsa_kernel _Z16sum_layer_kernelPKfS0_Pf
		.amdhsa_group_segment_fixed_size 18432
		.amdhsa_private_segment_fixed_size 0
		.amdhsa_kernarg_size 24
		.amdhsa_user_sgpr_count 2
		.amdhsa_user_sgpr_dispatch_ptr 0
		.amdhsa_user_sgpr_queue_ptr 0
		.amdhsa_user_sgpr_kernarg_segment_ptr 1
		.amdhsa_user_sgpr_dispatch_id 0
		.amdhsa_user_sgpr_kernarg_preload_length 0
		.amdhsa_user_sgpr_kernarg_preload_offset 0
		.amdhsa_user_sgpr_private_segment_size 0
		.amdhsa_uses_dynamic_stack 0
		.amdhsa_enable_private_segment 0
		.amdhsa_system_sgpr_workgroup_id_x 1
		.amdhsa_system_sgpr_workgroup_id_y 0
		.amdhsa_system_sgpr_workgroup_id_z 0
		.amdhsa_system_sgpr_workgroup_info 0
		.amdhsa_system_vgpr_workitem_id 0
		.amdhsa_next_free_vgpr 61
		.amdhsa_next_free_sgpr 19
		.amdhsa_accum_offset 64
		.amdhsa_reserve_vcc 1
		.amdhsa_float_round_mode_32 0
		.amdhsa_float_round_mode_16_64 0
		.amdhsa_float_denorm_mode_32 3
		.amdhsa_float_denorm_mode_16_64 3
		.amdhsa_dx10_clamp 1
		.amdhsa_ieee_mode 1
		.amdhsa_fp16_overflow 0
		.amdhsa_tg_split 0
		.amdhsa_exception_fp_ieee_invalid_op 0
		.amdhsa_exception_fp_denorm_src 0
		.amdhsa_exception_fp_ieee_div_zero 0
		.amdhsa_exception_fp_ieee_overflow 0
		.amdhsa_exception_fp_ieee_underflow 0
		.amdhsa_exception_fp_ieee_inexact 0
		.amdhsa_exception_int_div_zero 0
	.end_amdhsa_kernel

amdhsa.kernels:
  - .agpr_count:     0
    .args:
      - .address_space:  global
        .offset:         0
        .size:           8
        .value_kind:     global_buffer
      - .address_space:  global
        .offset:         8
        .size:           8
        .value_kind:     global_buffer
      - .address_space:  global
        .offset:         16
        .size:           8
        .value_kind:     global_buffer
    .group_segment_fixed_size: 18432
    .kernarg_segment_align: 8
    .kernarg_segment_size: 24
    .language:       OpenCL C
    .language_version:
      - 2
      - 0
    .max_flat_workgroup_size: 256
    .name:           _Z16sum_layer_kernelPKfS0_Pf
    .private_segment_fixed_size: 0
    .sgpr_count:     25
    .sgpr_spill_count: 0
    .symbol:         _Z16sum_layer_kernelPKfS0_Pf.kd
    .uniform_work_group_size: 1
    .uses_dynamic_stack: false
    .vgpr_count:     61
    .vgpr_spill_count: 0
    .wavefront_size: 64
